# v56 plus P3 group-norm row loop: the eight loop-invariant gain loads hoisted out of the loop into spare VGPRs (they were re-loaded behind every store, three dependent round trips per row)
# baseline (speedup 1.0000x reference)
.LBB0_356:
	s_load_dwordx8 s[84:91], s[2:3], 0x30
	v_and_b32_e32 v56, 63, v41
	s_andn2_b64 vcc, exec, s[4:5]
	v_mbcnt_lo_u32_b32 v1, -1, 0
	s_cbranch_vccnz .LBB0_360
	v_lshlrev_b32_e32 v55, 3, v41
	v_lshlrev_b32_e32 v2, 5, v56
	v_and_b32_e32 v3, 56, v55
	s_movk_i32 s4, 0x700
	v_and_or_b32 v4, v2, s4, v3
	v_mbcnt_hi_u32_b32 v2, -1, v1
	v_and_b32_e32 v5, 64, v2
	v_xor_b32_e32 v3, 1, v2
	v_add_u32_e32 v5, 64, v5
	v_cmp_lt_i32_e32 vcc, v3, v5
	s_load_dwordx2 s[2:3], s[2:3], 0x28
	v_readlane_b32 s4, v255, 10
	v_cndmask_b32_e32 v3, v2, v3, vcc
	v_lshlrev_b32_e32 v57, 2, v3
	v_xor_b32_e32 v3, 2, v2
	v_cmp_lt_i32_e32 vcc, v3, v5
	v_readlane_b32 s14, v255, 17
	v_readlane_b32 s15, v255, 18
	v_cndmask_b32_e32 v3, v2, v3, vcc
	v_lshlrev_b32_e32 v58, 2, v3
	v_xor_b32_e32 v3, 4, v2
	v_cmp_lt_i32_e32 vcc, v3, v5
	v_mov_b32_e32 v60, 0x358637bd
	s_mov_b32 s11, 0x800000
	v_cndmask_b32_e32 v2, v2, v3, vcc
	v_lshlrev_b32_e32 v59, 2, v2
	v_lshlrev_b32_e32 v2, 2, v4
	v_mov_b32_e32 v3, 0
	s_waitcnt lgkmcnt(0)
	v_lshl_add_u64 v[18:19], s[2:3], 0, v[2:3]
	s_ashr_i32 s2, s8, 31
	s_ashr_i32 s3, s4, 31
	s_add_u32 s6, s8, s4
	s_addc_u32 s7, s2, s3
	s_lshl_b64 s[2:3], s[6:7], 12
	s_add_u32 s2, s0, s2
	v_lshlrev_b32_e32 v2, 1, v4
	s_addc_u32 s3, s1, s3
	v_lshl_add_u64 v[4:5], s[2:3], 0, v[2:3]
	s_mov_b64 s[2:3], 0x1b300100
	s_ashr_i32 s15, s14, 31
	v_lshl_add_u64 v[20:21], v[4:5], 0, s[2:3]
	s_lshl_b64 s[2:3], s[14:15], 12
	s_lshl_b64 s[4:5], s[6:7], 13
	s_add_u32 s4, s0, s4
	s_addc_u32 s5, s1, s5
	v_lshl_add_u64 v[4:5], s[4:5], 0, v[2:3]
	s_mov_b64 s[4:5], 0x1d300100
	s_mulk_i32 s7, 0x6000
	s_mul_hi_u32 s10, s6, 0x6000
	v_lshl_add_u64 v[22:23], v[4:5], 0, s[4:5]
	s_lshl_b64 s[4:5], s[14:15], 13
	s_add_i32 s10, s10, s7
	s_mulk_i32 s6, 0x6000
	s_add_u32 s6, s0, s6
	s_addc_u32 s7, s1, s10
	v_lshl_add_u64 v[2:3], s[6:7], 0, v[2:3]
	s_mov_b64 s[6:7], 0xf303100
	v_lshl_add_u64 v[24:25], v[2:3], 0, s[6:7]
	s_mul_hi_i32 s7, s14, 0x6000
	s_mul_i32 s6, s14, 0x6000
	s_mov_b32 s10, 0xffff0000
	s_movk_i32 s12, 0x7fff
	global_load_dwordx4 v[200:203], v[18:19], off
	global_load_dwordx4 v[204:207], v[18:19], off offset:16
	global_load_dwordx4 v[208:211], v[18:19], off offset:256
	global_load_dwordx4 v[212:215], v[18:19], off offset:272
	global_load_dwordx4 v[216:219], v[18:19], off offset:512
	global_load_dwordx4 v[220:223], v[18:19], off offset:528
	global_load_dwordx4 v[224:227], v[18:19], off offset:768
	global_load_dwordx4 v[228:231], v[18:19], off offset:784
.LBB0_358:
	global_load_dwordx4 v[26:29], v[20:21], off offset:-256
	global_load_dwordx4 v[36:39], v[24:25], off offset:-256
	global_load_dwordx4 v[62:65], v[20:21], off offset:128
	global_load_dwordx4 v[66:69], v[20:21], off offset:-128
	global_load_dwordx4 v[70:73], v[24:25], off offset:-128
	global_load_dwordx4 v[74:77], v[20:21], off
	global_load_dwordx4 v[6:9], v[24:25], off
	global_load_dwordx4 v[2:5], v[24:25], off offset:128
	s_add_i32 s9, s9, s14
	v_lshl_add_u64 v[20:21], v[20:21], 0, s[2:3]
	v_lshl_add_u64 v[24:25], v[24:25], 0, s[6:7]
	s_cmpk_gt_i32 s9, 0x1fff
	s_waitcnt vmcnt(7)
	v_mov_b64_e32 v[14:15], v[200:201]
	v_mov_b64_e32 v[16:17], v[202:203]
	v_mov_b64_e32 v[10:11], v[204:205]
	v_mov_b64_e32 v[12:13], v[206:207]
	v_lshlrev_b32_e32 v52, 16, v26
	v_and_b32_e32 v26, 0xffff0000, v26
	v_add_f32_e32 v40, 0, v52
	v_lshlrev_b32_e32 v53, 16, v27
	v_add_f32_e32 v40, v40, v26
	v_and_b32_e32 v27, 0xffff0000, v27
	v_add_f32_e32 v40, v40, v53
	s_waitcnt vmcnt(6)
	v_mov_b32_e32 v34, v14
	v_lshlrev_b32_e32 v14, 16, v28
	v_add_f32_e32 v40, v40, v27
	v_and_b32_e32 v28, 0xffff0000, v28
	v_add_f32_e32 v40, v40, v14
	v_mov_b32_e32 v35, v16
	v_mov_b32_e32 v16, v15
	v_lshlrev_b32_e32 v15, 16, v29
	v_add_f32_e32 v40, v40, v28
	v_and_b32_e32 v29, 0xffff0000, v29
	v_add_f32_e32 v40, v40, v15
	s_waitcnt vmcnt(5)
	v_mov_b32_e32 v50, v10
	s_waitcnt vmcnt(4)
	v_lshlrev_b32_e32 v10, 16, v66
	v_add_f32_e32 v40, v40, v29
	v_lshlrev_b32_e32 v80, 16, v64
	v_and_b32_e32 v81, 0xffff0000, v64
	v_and_b32_e32 v64, 0xffff0000, v66
	v_add_f32_e32 v40, v40, v10
	v_mov_b32_e32 v51, v12
	v_mov_b32_e32 v12, v11
	v_lshlrev_b32_e32 v11, 16, v67
	v_add_f32_e32 v40, v40, v64
	v_lshlrev_b32_e32 v78, 16, v65
	v_and_b32_e32 v79, 0xffff0000, v65
	v_and_b32_e32 v65, 0xffff0000, v67
	v_add_f32_e32 v40, v40, v11
	v_lshlrev_b32_e32 v66, 16, v68
	v_add_f32_e32 v40, v40, v65
	v_and_b32_e32 v68, 0xffff0000, v68
	v_add_f32_e32 v40, v40, v66
	v_lshlrev_b32_e32 v67, 16, v69
	v_add_f32_e32 v40, v40, v68
	v_and_b32_e32 v69, 0xffff0000, v69
	v_add_f32_e32 v40, v40, v67
	v_lshlrev_b32_e32 v30, 16, v36
	v_and_b32_e32 v32, 0xffff0000, v36
	v_lshlrev_b32_e32 v42, 16, v38
	v_and_b32_e32 v46, 0xffff0000, v38
	s_waitcnt vmcnt(3)
	v_lshlrev_b32_e32 v36, 16, v70
	v_and_b32_e32 v38, 0xffff0000, v70
	s_waitcnt vmcnt(2)
	v_lshlrev_b32_e32 v70, 16, v74
	v_add_f32_e32 v40, v40, v69
	v_lshlrev_b32_e32 v44, 16, v72
	v_and_b32_e32 v48, 0xffff0000, v72
	v_and_b32_e32 v72, 0xffff0000, v74
	v_add_f32_e32 v40, v40, v70
	v_lshlrev_b32_e32 v31, 16, v37
	v_and_b32_e32 v33, 0xffff0000, v37
	v_lshlrev_b32_e32 v43, 16, v39
	v_and_b32_e32 v47, 0xffff0000, v39
	v_lshlrev_b32_e32 v37, 16, v71
	v_and_b32_e32 v39, 0xffff0000, v71
	v_lshlrev_b32_e32 v71, 16, v75
	v_add_f32_e32 v40, v40, v72
	v_lshlrev_b32_e32 v45, 16, v73
	v_and_b32_e32 v49, 0xffff0000, v73
	v_and_b32_e32 v73, 0xffff0000, v75
	v_add_f32_e32 v40, v40, v71
	v_lshlrev_b32_e32 v74, 16, v76
	v_add_f32_e32 v40, v40, v73
	v_and_b32_e32 v76, 0xffff0000, v76
	v_add_f32_e32 v40, v40, v74
	v_lshlrev_b32_e32 v75, 16, v77
	v_add_f32_e32 v40, v40, v76
	v_and_b32_e32 v77, 0xffff0000, v77
	v_add_f32_e32 v40, v40, v75
	v_lshlrev_b32_e32 v82, 16, v62
	v_add_f32_e32 v40, v40, v77
	v_and_b32_e32 v62, 0xffff0000, v62
	v_add_f32_e32 v40, v40, v82
	v_lshlrev_b32_e32 v83, 16, v63
	v_add_f32_e32 v40, v40, v62
	v_and_b32_e32 v63, 0xffff0000, v63
	v_add_f32_e32 v40, v40, v83
	v_add_f32_e32 v40, v40, v63
	v_add_f32_e32 v40, v40, v80
	v_add_f32_e32 v40, v40, v81
	v_add_f32_e32 v40, v40, v78
	v_add_f32_e32 v40, v40, v79
	ds_bpermute_b32 v61, v57, v40
	s_waitcnt lgkmcnt(0)
	v_add_f32_e32 v40, v40, v61
	ds_bpermute_b32 v61, v58, v40
	s_waitcnt lgkmcnt(0)
	v_add_f32_e32 v40, v40, v61
	ds_bpermute_b32 v61, v59, v40
	s_waitcnt lgkmcnt(0)
	v_add_f32_e32 v40, v40, v61
	v_mul_f32_e32 v40, 0x3b800000, v40
	v_pk_add_f32 v[84:85], v[52:53], v[40:41] op_sel_hi:[1,0] neg_lo:[0,1] neg_hi:[0,1]
	v_pk_add_f32 v[86:87], v[26:27], v[40:41] op_sel_hi:[1,0] neg_lo:[0,1] neg_hi:[0,1]
	v_pk_add_f32 v[88:89], v[14:15], v[40:41] op_sel_hi:[1,0] neg_lo:[0,1] neg_hi:[0,1]
	v_pk_add_f32 v[52:53], v[76:77], v[40:41] op_sel_hi:[1,0] neg_lo:[0,1] neg_hi:[0,1]
	v_pk_add_f32 v[14:15], v[62:63], v[40:41] op_sel_hi:[1,0] neg_lo:[0,1] neg_hi:[0,1]
	v_pk_mul_f32 v[62:63], v[84:85], v[84:85]
	v_pk_mul_f32 v[76:77], v[86:87], v[86:87]
	v_pk_add_f32 v[90:91], v[28:29], v[40:41] op_sel_hi:[1,0] neg_lo:[0,1] neg_hi:[0,1]
	v_pk_add_f32 v[92:93], v[10:11], v[40:41] op_sel_hi:[1,0] neg_lo:[0,1] neg_hi:[0,1]
	v_pk_add_f32 v[64:65], v[64:65], v[40:41] op_sel_hi:[1,0] neg_lo:[0,1] neg_hi:[0,1]
	v_pk_add_f32 v[66:67], v[66:67], v[40:41] op_sel_hi:[1,0] neg_lo:[0,1] neg_hi:[0,1]
	v_pk_add_f32 v[68:69], v[68:69], v[40:41] op_sel_hi:[1,0] neg_lo:[0,1] neg_hi:[0,1]
	v_pk_add_f32 v[70:71], v[70:71], v[40:41] op_sel_hi:[1,0] neg_lo:[0,1] neg_hi:[0,1]
	v_pk_add_f32 v[72:73], v[72:73], v[40:41] op_sel_hi:[1,0] neg_lo:[0,1] neg_hi:[0,1]
	v_pk_add_f32 v[74:75], v[74:75], v[40:41] op_sel_hi:[1,0] neg_lo:[0,1] neg_hi:[0,1]
	v_pk_add_f32 v[10:11], v[82:83], v[40:41] op_sel_hi:[1,0] neg_lo:[0,1] neg_hi:[0,1]
	v_pk_add_f32 v[28:29], v[80:81], v[40:41] op_sel_hi:[1,0] neg_lo:[0,1] neg_hi:[0,1]
	v_pk_add_f32 v[26:27], v[78:79], v[40:41] op_sel_hi:[1,0] neg_lo:[0,1] neg_hi:[0,1]
	v_add_f32_e32 v40, v62, v76
	v_add_f32_e32 v40, v40, v63
	v_pk_mul_f32 v[78:79], v[88:89], v[88:89]
	v_add_f32_e32 v40, v40, v77
	v_pk_mul_f32 v[80:81], v[90:91], v[90:91]
	v_add_f32_e32 v40, v40, v78
	v_add_f32_e32 v40, v40, v80
	v_add_f32_e32 v40, v40, v79
	v_pk_mul_f32 v[82:83], v[92:93], v[92:93]
	v_add_f32_e32 v40, v40, v81
	v_pk_mul_f32 v[94:95], v[64:65], v[64:65]
	v_add_f32_e32 v40, v40, v82
	v_add_f32_e32 v40, v40, v94
	v_add_f32_e32 v40, v40, v83
	v_pk_mul_f32 v[96:97], v[66:67], v[66:67]
	v_add_f32_e32 v40, v40, v95
	v_pk_mul_f32 v[98:99], v[68:69], v[68:69]
	v_add_f32_e32 v40, v40, v96
	v_add_f32_e32 v40, v40, v98
	v_add_f32_e32 v40, v40, v97
	v_pk_mul_f32 v[100:101], v[70:71], v[70:71]
	v_add_f32_e32 v40, v40, v99
	v_pk_mul_f32 v[102:103], v[72:73], v[72:73]
	v_add_f32_e32 v40, v40, v100
	v_add_f32_e32 v40, v40, v102
	v_add_f32_e32 v40, v40, v101
	v_pk_mul_f32 v[104:105], v[74:75], v[74:75]
	v_add_f32_e32 v40, v40, v103
	v_pk_mul_f32 v[106:107], v[52:53], v[52:53]
	v_add_f32_e32 v40, v40, v104
	v_add_f32_e32 v40, v40, v106
	v_mov_b32_e32 v108, v10
	v_mov_b32_e32 v109, v14
	v_add_f32_e32 v40, v40, v105
	v_pk_mul_f32 v[108:109], v[108:109], v[108:109]
	v_add_f32_e32 v40, v40, v107
	v_mov_b32_e32 v110, v11
	v_mov_b32_e32 v111, v15
	v_add_f32_e32 v40, v40, v108
	v_pk_mul_f32 v[110:111], v[110:111], v[110:111]
	v_add_f32_e32 v40, v40, v109
	v_add_f32_e32 v40, v40, v110
	v_pk_mul_f32 v[112:113], v[28:29], v[28:29]
	v_add_f32_e32 v40, v40, v111
	v_add_f32_e32 v40, v40, v112
	v_pk_mul_f32 v[114:115], v[26:27], v[26:27]
	v_add_f32_e32 v40, v40, v113
	v_add_f32_e32 v40, v40, v114
	v_add_f32_e32 v40, v40, v115
	ds_bpermute_b32 v61, v57, v40
	s_waitcnt lgkmcnt(0)
	v_add_f32_e32 v40, v40, v61
	ds_bpermute_b32 v61, v58, v40
	s_waitcnt lgkmcnt(0)
	v_add_f32_e32 v40, v40, v61
	ds_bpermute_b32 v61, v59, v40
	s_waitcnt lgkmcnt(0)
	v_add_f32_e32 v40, v40, v61
	v_fmamk_f32 v40, v40, 0x3b800000, v60
	v_mul_f32_e32 v61, 0x4b800000, v40
	v_cmp_gt_f32_e32 vcc, s11, v40
	s_nop 1
	v_cndmask_b32_e32 v40, v40, v61, vcc
	v_rsq_f32_e32 v40, v40
	s_nop 0
	v_mul_f32_e32 v61, 0x45800000, v40
	v_cndmask_b32_e32 v40, v40, v61, vcc
	v_pk_mul_f32 v[62:63], v[40:41], v[84:85] op_sel_hi:[0,1]
	v_pk_mul_f32 v[76:77], v[40:41], v[86:87] op_sel_hi:[0,1]
	v_pk_mul_f32 v[78:79], v[40:41], v[88:89] op_sel_hi:[0,1]
	v_pk_mul_f32 v[80:81], v[40:41], v[90:91] op_sel_hi:[0,1]
	v_pk_mul_f32 v[34:35], v[62:63], v[34:35]
	v_pk_mul_f32 v[16:17], v[76:77], v[16:17]
	v_pk_mul_f32 v[50:51], v[78:79], v[50:51]
	v_pk_mul_f32 v[12:13], v[80:81], v[12:13]
	v_pk_mul_f32 v[30:31], v[34:35], v[30:31]
	v_pk_mul_f32 v[16:17], v[16:17], v[32:33]
	v_pk_mul_f32 v[32:33], v[50:51], v[42:43]
	v_pk_mul_f32 v[12:13], v[12:13], v[46:47]
	v_bfe_u32 v46, v30, 16, 1
	v_bfe_u32 v47, v31, 16, 1
	v_bfe_u32 v50, v32, 16, 1
	v_bfe_u32 v51, v33, 16, 1
	v_bfe_u32 v34, v13, 16, 1
	v_bfe_u32 v35, v12, 16, 1
	v_bfe_u32 v42, v17, 16, 1
	v_bfe_u32 v43, v16, 16, 1
	v_add3_u32 v33, v33, v51, s12
	v_add3_u32 v32, v32, v50, s12
	v_add3_u32 v31, v31, v47, s12
	v_add3_u32 v30, v30, v46, s12
	v_add3_u32 v16, v16, v43, s12
	v_add3_u32 v17, v17, v42, s12
	v_add3_u32 v12, v12, v35, s12
	v_add3_u32 v13, v13, v34, s12
	v_lshrrev_b32_e32 v30, 16, v30
	v_lshrrev_b32_e32 v31, 16, v31
	v_lshrrev_b32_e32 v32, 16, v32
	v_lshrrev_b32_e32 v33, 16, v33
	v_and_or_b32 v33, v13, s10, v33
	v_and_or_b32 v32, v12, s10, v32
	v_and_or_b32 v31, v17, s10, v31
	v_and_or_b32 v30, v16, s10, v30
	global_store_dwordx4 v[22:23], v[30:33], off offset:-256
	s_nop 1
	v_pk_mul_f32 v[84:85], v[40:41], v[64:65] op_sel_hi:[0,1]
	v_mov_b64_e32 v[30:31], v[208:209]
	v_mov_b64_e32 v[32:33], v[210:211]
	v_mov_b64_e32 v[62:63], v[212:213]
	v_mov_b64_e32 v[64:65], v[214:215]
	v_pk_mul_f32 v[82:83], v[40:41], v[92:93] op_sel_hi:[0,1]
	v_pk_mul_f32 v[66:67], v[40:41], v[66:67] op_sel_hi:[0,1]
	v_pk_mul_f32 v[68:69], v[40:41], v[68:69] op_sel_hi:[0,1]
	v_pk_mul_f32 v[46:47], v[40:41], v[52:53] op_sel_hi:[0,1]
	v_pk_mul_f32 v[10:11], v[40:41], v[10:11] op_sel_hi:[0,1]
	v_pk_mul_f32 v[14:15], v[40:41], v[14:15] op_sel_hi:[0,1]
	s_waitcnt vmcnt(1)
	v_mov_b32_e32 v12, v30
	v_mov_b32_e32 v13, v32
	v_mov_b32_e32 v16, v62
	v_mov_b32_e32 v17, v64
	v_mov_b32_e32 v32, v31
	v_mov_b32_e32 v64, v63
	v_pk_mul_f32 v[12:13], v[82:83], v[12:13]
	v_pk_mul_f32 v[16:17], v[66:67], v[16:17]
	v_pk_mul_f32 v[30:31], v[84:85], v[32:33]
	v_pk_mul_f32 v[32:33], v[68:69], v[64:65]
	v_pk_mul_f32 v[12:13], v[12:13], v[36:37]
	v_pk_mul_f32 v[16:17], v[16:17], v[44:45]
	v_pk_mul_f32 v[30:31], v[30:31], v[38:39]
	v_pk_mul_f32 v[32:33], v[32:33], v[48:49]
	v_bfe_u32 v38, v12, 16, 1
	v_bfe_u32 v39, v13, 16, 1
	v_bfe_u32 v42, v16, 16, 1
	v_bfe_u32 v43, v17, 16, 1
	v_bfe_u32 v34, v33, 16, 1
	v_bfe_u32 v35, v32, 16, 1
	v_bfe_u32 v36, v31, 16, 1
	v_bfe_u32 v37, v30, 16, 1
	v_add3_u32 v17, v17, v43, s12
	v_add3_u32 v16, v16, v42, s12
	v_add3_u32 v13, v13, v39, s12
	v_add3_u32 v12, v12, v38, s12
	v_add3_u32 v30, v30, v37, s12
	v_add3_u32 v31, v31, v36, s12
	v_add3_u32 v32, v32, v35, s12
	v_add3_u32 v33, v33, v34, s12
	v_lshrrev_b32_e32 v12, 16, v12
	v_lshrrev_b32_e32 v13, 16, v13
	v_lshrrev_b32_e32 v16, 16, v16
	v_lshrrev_b32_e32 v17, 16, v17
	v_and_or_b32 v33, v33, s10, v17
	v_and_or_b32 v32, v32, s10, v16
	v_and_or_b32 v31, v31, s10, v13
	v_and_or_b32 v30, v30, s10, v12
	global_store_dwordx4 v[22:23], v[30:33], off offset:-128
	s_nop 1
	v_mov_b64_e32 v[30:31], v[216:217]
	v_mov_b64_e32 v[32:33], v[218:219]
	s_nop 0
	v_mov_b64_e32 v[34:35], v[220:221]
	v_mov_b64_e32 v[36:37], v[222:223]
	v_pk_mul_f32 v[38:39], v[40:41], v[70:71] op_sel_hi:[0,1]
	v_pk_mul_f32 v[44:45], v[40:41], v[74:75] op_sel_hi:[0,1]
	v_lshlrev_b32_e32 v13, 16, v7
	v_lshlrev_b32_e32 v12, 16, v6
	v_lshlrev_b32_e32 v17, 16, v9
	v_lshlrev_b32_e32 v16, 16, v8
	v_pk_mul_f32 v[42:43], v[40:41], v[72:73] op_sel_hi:[0,1]
	v_and_b32_e32 v7, 0xffff0000, v7
	v_and_b32_e32 v6, 0xffff0000, v6
	v_and_b32_e32 v9, 0xffff0000, v9
	v_and_b32_e32 v8, 0xffff0000, v8
	v_mov_b32_e32 v48, v30
	v_mov_b32_e32 v49, v32
	v_mov_b32_e32 v32, v31
	v_mov_b32_e32 v30, v34
	v_mov_b32_e32 v31, v36
	v_mov_b32_e32 v36, v35
	v_pk_mul_f32 v[34:35], v[38:39], v[48:49]
	v_pk_mul_f32 v[30:31], v[44:45], v[30:31]
	v_pk_mul_f32 v[32:33], v[42:43], v[32:33]
	v_pk_mul_f32 v[36:37], v[46:47], v[36:37]
	v_pk_mul_f32 v[12:13], v[34:35], v[12:13]
	v_pk_mul_f32 v[16:17], v[30:31], v[16:17]
	v_pk_mul_f32 v[6:7], v[32:33], v[6:7]
	v_pk_mul_f32 v[8:9], v[36:37], v[8:9]
	v_bfe_u32 v34, v12, 16, 1
	v_bfe_u32 v35, v13, 16, 1
	v_bfe_u32 v36, v16, 16, 1
	v_bfe_u32 v37, v17, 16, 1
	v_bfe_u32 v30, v9, 16, 1
	v_bfe_u32 v31, v8, 16, 1
	v_bfe_u32 v32, v7, 16, 1
	v_bfe_u32 v33, v6, 16, 1
	v_add3_u32 v17, v17, v37, s12
	v_add3_u32 v16, v16, v36, s12
	v_add3_u32 v13, v13, v35, s12
	v_add3_u32 v12, v12, v34, s12
	v_add3_u32 v6, v6, v33, s12
	v_add3_u32 v7, v7, v32, s12
	v_add3_u32 v8, v8, v31, s12
	v_add3_u32 v9, v9, v30, s12
	v_lshrrev_b32_e32 v12, 16, v12
	v_lshrrev_b32_e32 v13, 16, v13
	v_lshrrev_b32_e32 v16, 16, v16
	v_lshrrev_b32_e32 v17, 16, v17
	v_and_or_b32 v9, v9, s10, v17
	v_and_or_b32 v8, v8, s10, v16
	v_and_or_b32 v7, v7, s10, v13
	v_and_or_b32 v6, v6, s10, v12
	global_store_dwordx4 v[22:23], v[6:9], off
	s_nop 1
	v_mov_b64_e32 v[6:7], v[224:225]
	v_mov_b64_e32 v[8:9], v[226:227]
	s_nop 0
	v_mov_b64_e32 v[30:31], v[228:229]
	v_mov_b64_e32 v[32:33], v[230:231]
	v_mov_b32_e32 v34, v28
	v_mov_b32_e32 v35, v26
	v_mov_b32_e32 v26, v29
	v_pk_mul_f32 v[28:29], v[40:41], v[34:35] op_sel_hi:[0,1]
	v_pk_mul_f32 v[26:27], v[40:41], v[26:27] op_sel_hi:[0,1]
	v_lshlrev_b32_e32 v13, 16, v3
	v_lshlrev_b32_e32 v12, 16, v2
	v_lshlrev_b32_e32 v17, 16, v5
	v_lshlrev_b32_e32 v16, 16, v4
	v_and_b32_e32 v5, 0xffff0000, v5
	v_and_b32_e32 v4, 0xffff0000, v4
	v_and_b32_e32 v3, 0xffff0000, v3
	v_and_b32_e32 v2, 0xffff0000, v2
	v_mov_b32_e32 v34, v6
	v_mov_b32_e32 v35, v8
	v_mov_b32_e32 v8, v7
	v_mov_b32_e32 v6, v30
	v_mov_b32_e32 v7, v32
	v_mov_b32_e32 v32, v31
	v_pk_mul_f32 v[10:11], v[10:11], v[34:35]
	v_pk_mul_f32 v[8:9], v[14:15], v[8:9]
	v_pk_mul_f32 v[6:7], v[28:29], v[6:7]
	v_pk_mul_f32 v[14:15], v[26:27], v[32:33]
	v_pk_mul_f32 v[10:11], v[10:11], v[12:13]
	v_pk_mul_f32 v[6:7], v[6:7], v[16:17]
	v_pk_mul_f32 v[4:5], v[14:15], v[4:5]
	v_pk_mul_f32 v[2:3], v[8:9], v[2:3]
	v_bfe_u32 v8, v5, 16, 1
	v_bfe_u32 v9, v4, 16, 1
	v_bfe_u32 v14, v10, 16, 1
	v_bfe_u32 v15, v11, 16, 1
	v_bfe_u32 v16, v6, 16, 1
	v_bfe_u32 v17, v7, 16, 1
	v_bfe_u32 v12, v3, 16, 1
	v_bfe_u32 v13, v2, 16, 1
	v_add3_u32 v4, v4, v9, s12
	v_add3_u32 v5, v5, v8, s12
	v_add3_u32 v7, v7, v17, s12
	v_add3_u32 v6, v6, v16, s12
	v_add3_u32 v8, v11, v15, s12
	v_add3_u32 v9, v10, v14, s12
	v_add3_u32 v2, v2, v13, s12
	v_add3_u32 v3, v3, v12, s12
	v_lshrrev_b32_e32 v9, 16, v9
	v_lshrrev_b32_e32 v8, 16, v8
	v_lshrrev_b32_e32 v6, 16, v6
	v_lshrrev_b32_e32 v7, 16, v7
	v_and_or_b32 v5, v5, s10, v7
	v_and_or_b32 v4, v4, s10, v6
	v_and_or_b32 v3, v3, s10, v8
	v_and_or_b32 v2, v2, s10, v9
	global_store_dwordx4 v[22:23], v[2:5], off offset:128
	v_lshl_add_u64 v[22:23], v[22:23], 0, s[4:5]
	s_cbranch_scc0 .LBB0_358
	v_writelane_b32 v255, s14, 17
	s_nop 1
	v_writelane_b32 v255, s15, 18
